# baseline (speedup 1.0000x reference)
.LBB2_21:
	v_cvt_pk_f16_f32 v13, v13, v13
	v_cvt_pk_f16_f32 v12, v12, v12
	v_cvt_pk_f16_f32 v11, v11, v11
	v_cvt_pk_f16_f32 v10, v10, v10
	ds_write_b128 v98, v[10:13]
	ds_write_b32 v98, v17 offset:16
	s_and_saveexec_b64 s[6:7], s[4:5]
	ds_write_b32 v99, v86 offset:16
	s_or_b64 exec, exec, s[6:7]
	s_sub_i32 s6, s23, s24
	s_cmp_lt_i32 s6, 1
	s_cbranch_scc1 .LBB2_26
	ds_read2_b32 v[6:7], v96 offset0:20 offset1:28
	ds_read2_b32 v[8:9], v96 offset0:4 offset1:12
	s_min_i32 s6, s6, 16
	s_mov_b32 s7, 0
	v_mov_b32_e32 v118, v96
	v_subrev_u32_e32 v119, s24, v79
	v_mov_b32_e32 v10, 0
	v_mov_b32_e32 v11, 0
	v_mov_b32_e32 v12, 0
	v_mov_b32_e32 v13, 0
	v_mov_b32_e32 v14, 0
	v_mov_b32_e32 v15, 0
	v_mov_b32_e32 v16, 0
	v_mov_b32_e32 v17, 0
	v_mov_b32_e32 v54, 0
	v_mov_b32_e32 v55, 0
	v_mov_b32_e32 v56, 0
	v_mov_b32_e32 v57, 0
	v_mov_b32_e32 v58, 0
	v_mov_b32_e32 v59, 0
	v_mov_b32_e32 v60, 0
	v_mov_b32_e32 v61, 0
	s_waitcnt lgkmcnt(0)
	v_lshl_or_b32 v8, v8, 8, v72
	v_lshl_or_b32 v9, v9, 8, v72
	v_lshl_or_b32 v6, v6, 8, v72
	v_lshl_or_b32 v7, v7, 8, v72
	v_cmp_lt_i32_e32 vcc, 0, v119
	s_mov_b64 exec, vcc
	global_load_dwordx4 v[14:17], v8, s[16:17]
	s_mov_b64 exec, -1
	v_cmp_lt_i32_e32 vcc, 1, v119
	s_mov_b64 exec, vcc
	global_load_dwordx4 v[10:13], v9, s[16:17]
	s_mov_b64 exec, -1
	v_cmp_lt_i32_e32 vcc, 2, v119
	s_mov_b64 exec, vcc
	global_load_dwordx4 v[54:57], v6, s[16:17]
	s_mov_b64 exec, -1
	v_cmp_lt_i32_e32 vcc, 3, v119
	s_mov_b64 exec, vcc
	global_load_dwordx4 v[58:61], v7, s[16:17]
	s_mov_b64 exec, -1
	v_add_u32_e32 v119, -4, v119
.LBB2_25:
	ds_read_b128 v[120:123], v118
	ds_read_b128 v[124:127], v118 offset:32
	ds_read2_b32 v[6:7], v118 offset0:36 offset1:44
	s_add_i32 s7, s7, 4
	s_waitcnt vmcnt(3) lgkmcnt(2)
	v_pk_fma_f16 v109, v14, v120, v109
	v_pk_fma_f16 v97, v14, v121, v97
	v_pk_fma_f16 v90, v14, v122, v90
	v_pk_fma_f16 v85, v14, v123, v85
	v_pk_fma_f16 v108, v15, v120, v108
	v_pk_fma_f16 v95, v15, v121, v95
	v_pk_fma_f16 v89, v15, v122, v89
	v_pk_fma_f16 v84, v15, v123, v84
	v_pk_fma_f16 v107, v16, v120, v107
	v_pk_fma_f16 v94, v16, v121, v94
	v_pk_fma_f16 v88, v16, v122, v88
	v_pk_fma_f16 v82, v16, v123, v82
	v_pk_fma_f16 v105, v17, v120, v105
	v_pk_fma_f16 v92, v17, v121, v92
	v_pk_fma_f16 v87, v17, v122, v87
	v_pk_fma_f16 v81, v17, v123, v81
	s_waitcnt lgkmcnt(0)
	v_lshl_or_b32 v6, v6, 8, v72
	v_cmp_lt_i32_e32 vcc, 0, v119
	s_mov_b64 exec, vcc
	global_load_dwordx4 v[14:17], v6, s[16:17]
	s_mov_b64 exec, -1
	ds_read_b128 v[120:123], v118 offset:64
	s_waitcnt vmcnt(3)
	v_pk_fma_f16 v109, v10, v124, v109
	v_pk_fma_f16 v97, v10, v125, v97
	v_pk_fma_f16 v90, v10, v126, v90
	v_pk_fma_f16 v85, v10, v127, v85
	v_pk_fma_f16 v108, v11, v124, v108
	v_pk_fma_f16 v95, v11, v125, v95
	v_pk_fma_f16 v89, v11, v126, v89
	v_pk_fma_f16 v84, v11, v127, v84
	v_pk_fma_f16 v107, v12, v124, v107
	v_pk_fma_f16 v94, v12, v125, v94
	v_pk_fma_f16 v88, v12, v126, v88
	v_pk_fma_f16 v82, v12, v127, v82
	v_pk_fma_f16 v105, v13, v124, v105
	v_pk_fma_f16 v92, v13, v125, v92
	v_pk_fma_f16 v87, v13, v126, v87
	v_pk_fma_f16 v81, v13, v127, v81
	v_lshl_or_b32 v7, v7, 8, v72
	v_cmp_lt_i32_e32 vcc, 1, v119
	s_mov_b64 exec, vcc
	global_load_dwordx4 v[10:13], v7, s[16:17]
	s_mov_b64 exec, -1
	ds_read2_b32 v[8:9], v118 offset0:52 offset1:60
	ds_read_b128 v[124:127], v118 offset:96
	s_waitcnt vmcnt(3) lgkmcnt(2)
	v_pk_fma_f16 v109, v54, v120, v109
	v_pk_fma_f16 v97, v54, v121, v97
	v_pk_fma_f16 v90, v54, v122, v90
	v_pk_fma_f16 v85, v54, v123, v85
	v_pk_fma_f16 v108, v55, v120, v108
	v_pk_fma_f16 v95, v55, v121, v95
	v_pk_fma_f16 v89, v55, v122, v89
	v_pk_fma_f16 v84, v55, v123, v84
	v_pk_fma_f16 v107, v56, v120, v107
	v_pk_fma_f16 v94, v56, v121, v94
	v_pk_fma_f16 v88, v56, v122, v88
	v_pk_fma_f16 v82, v56, v123, v82
	v_pk_fma_f16 v105, v57, v120, v105
	v_pk_fma_f16 v92, v57, v121, v92
	v_pk_fma_f16 v87, v57, v122, v87
	v_pk_fma_f16 v81, v57, v123, v81
	s_waitcnt lgkmcnt(1)
	v_lshl_or_b32 v8, v8, 8, v72
	v_cmp_lt_i32_e32 vcc, 2, v119
	s_mov_b64 exec, vcc
	global_load_dwordx4 v[54:57], v8, s[16:17]
	s_mov_b64 exec, -1
	v_add_u32_e32 v118, 0x80, v118
	s_waitcnt vmcnt(3) lgkmcnt(0)
	v_pk_fma_f16 v109, v58, v124, v109
	v_pk_fma_f16 v97, v58, v125, v97
	v_pk_fma_f16 v90, v58, v126, v90
	v_pk_fma_f16 v85, v58, v127, v85
	v_pk_fma_f16 v108, v59, v124, v108
	v_pk_fma_f16 v95, v59, v125, v95
	v_pk_fma_f16 v89, v59, v126, v89
	v_pk_fma_f16 v84, v59, v127, v84
	v_pk_fma_f16 v107, v60, v124, v107
	v_pk_fma_f16 v94, v60, v125, v94
	v_pk_fma_f16 v88, v60, v126, v88
	v_pk_fma_f16 v82, v60, v127, v82
	v_pk_fma_f16 v105, v61, v124, v105
	v_pk_fma_f16 v92, v61, v125, v92
	v_pk_fma_f16 v87, v61, v126, v87
	v_pk_fma_f16 v81, v61, v127, v81
	v_lshl_or_b32 v9, v9, 8, v72
	v_cmp_lt_i32_e32 vcc, 3, v119
	s_mov_b64 exec, vcc
	global_load_dwordx4 v[58:61], v9, s[16:17]
	s_mov_b64 exec, -1
	v_add_u32_e32 v119, -4, v119
	s_cmp_ge_i32 s7, s6
	s_cbranch_scc0 .LBB2_25
